# v15: FOX attention starts from the per-row upper-bound reference (decay bias at the row + QK-norm bound), so no running-max rescale; runtime check with fallback
# speedup vs baseline: 1.0207x; 1.0207x over previous
; template <bool FOX>
; __device__ __forceinline__ void attn_unit(const Args& A, int b, int h, int qb, LAS char* shm, LAS float* dg) {
;     ...
;         float gq = fmaxf(fabsf(A.gfq[lane]), 0.f), gk = fabsf(A.gfk[lane]);
; #pragma unroll
;         for (int o = 32; o > 0; o >>= 1) { gq = fmaxf(gq, __shfl_xor(gq, o)); gk = fmaxf(gk, __shfl_xor(gk, o)); }
;         const float margin = 2.f * (8.f * gq * gk) + SKIP_NATS;
;         const float Fref = A.F[(rowbase + q0) * 8 + h];
.LBB0_926:
	s_or_b64 exec, exec, s[12:13]
	s_bitcmp0_b32 s3, 0
	s_cselect_b64 s[4:5], -1, 0
	s_cmp_ge_i32 s2, s74
	s_cselect_b64 s[6:7], -1, 0
	s_or_b64 s[4:5], s[4:5], s[6:7]
	s_mov_b64 s[12:13], -1
	s_and_b64 vcc, exec, s[4:5]
	s_cbranch_vccz .LBB0_1017
	v_mov_b32_e32 v128, v0
	v_and_b32_e32 v6, 64, v237
	v_and_b32_e32 v191, 63, v128
	v_lshlrev_b32_e32 v3, 2, v191
	global_load_dword v4, v3, s[36:37]
	v_add_u32_e32 v6, 64, v6
	global_load_dword v3, v3, s[88:89]
	v_xor_b32_e32 v7, 32, v237
	v_cmp_lt_i32_e32 vcc, v7, v6
	s_not_b32 s3, s1
	s_bfe_u32 s3, s3, 0x50002
	v_cndmask_b32_e32 v7, v237, v7, vcc
	v_lshlrev_b32_e32 v7, 2, v7
	s_and_b32 s4, s1, 3
	s_lshl_b32 s6, s4, 13
	s_lshl_b32 s5, s3, 8
	s_or_b32 s8, s5, s6
	s_ashr_i32 s1, s0, 31
	s_lshl_b32 s8, s8, 5
	s_add_u32 s8, s34, s8
	s_addc_u32 s15, s35, 0
	s_lshl_b64 s[12:13], s[0:1], 2
	s_add_u32 s14, s8, s12
	s_addc_u32 s15, s15, s13
	s_lshl_b32 s3, s3, 2
	v_readfirstlane_b32 s7, v128
	s_mov_b64 s[18:19], -1
	s_waitcnt vmcnt(1)
	v_max_f32_e64 v4, |v4|, |v4|
	v_max_f32_e32 v4, 0, v4
	s_waitcnt vmcnt(0)
	v_and_b32_e32 v5, 0x7fffffff, v3
	ds_bpermute_b32 v5, v7, v5
	ds_bpermute_b32 v8, v7, v4
	v_max_f32_e64 v3, |v3|, |v3|
	s_waitcnt lgkmcnt(1)
	v_max_f32_e32 v5, v5, v5
	v_max_f32_e32 v3, v3, v5
	v_xor_b32_e32 v5, 16, v237
	v_cmp_lt_i32_e32 vcc, v5, v6
	s_waitcnt lgkmcnt(0)
	v_max_f32_e32 v8, v8, v8
	v_max_f32_e32 v4, v4, v8
	v_cndmask_b32_e32 v5, v237, v5, vcc
	v_lshlrev_b32_e32 v5, 2, v5
	ds_bpermute_b32 v7, v5, v4
	ds_bpermute_b32 v5, v5, v3
	s_waitcnt lgkmcnt(1)
	v_max_f32_e32 v7, v7, v7
	s_waitcnt lgkmcnt(0)
	v_max_f32_e32 v5, v5, v5
	v_max_f32_e32 v3, v3, v5
	v_xor_b32_e32 v5, 8, v237
	v_cmp_lt_i32_e32 vcc, v5, v6
	v_max_f32_e32 v4, v4, v7
	s_nop 0
	v_cndmask_b32_e32 v5, v237, v5, vcc
	v_lshlrev_b32_e32 v5, 2, v5
	ds_bpermute_b32 v7, v5, v4
	ds_bpermute_b32 v5, v5, v3
	s_waitcnt lgkmcnt(1)
	v_max_f32_e32 v7, v7, v7
	s_waitcnt lgkmcnt(0)
	v_max_f32_e32 v5, v5, v5
	v_max_f32_e32 v5, v3, v5
	v_xor_b32_e32 v3, 4, v237
	v_cmp_lt_i32_e32 vcc, v3, v6
	v_max_f32_e32 v4, v4, v7
	s_nop 0
	v_cndmask_b32_e32 v3, v237, v3, vcc
	v_lshlrev_b32_e32 v3, 2, v3
	ds_bpermute_b32 v7, v3, v4
	s_waitcnt lgkmcnt(0)
	v_max_f32_e32 v7, v7, v7
	v_max_f32_e32 v4, v4, v7
	ds_bpermute_b32 v7, v3, v5
	s_waitcnt lgkmcnt(0)
	v_max_f32_e32 v7, v7, v7
	v_max_f32_e32 v5, v5, v7
	v_xor_b32_e32 v7, 2, v237
	v_cmp_lt_i32_e32 vcc, v7, v6
	s_nop 1
	v_cndmask_b32_e32 v7, v237, v7, vcc
	v_lshlrev_b32_e32 v134, 2, v7
	ds_bpermute_b32 v7, v134, v4
	s_waitcnt lgkmcnt(0)
	v_max_f32_e32 v7, v7, v7
	v_max_f32_e32 v4, v4, v7
	ds_bpermute_b32 v7, v134, v5
	s_waitcnt lgkmcnt(0)
	v_max_f32_e32 v7, v7, v7
	v_max_f32_e32 v5, v5, v7
	v_xor_b32_e32 v7, 1, v237
	v_cmp_lt_i32_e32 vcc, v7, v6
	s_nop 1
	v_cndmask_b32_e32 v6, v237, v7, vcc
	v_lshlrev_b32_e32 v190, 2, v6
	ds_bpermute_b32 v6, v190, v4
	v_cmp_gt_u32_e32 vcc, s3, v191
	s_waitcnt lgkmcnt(0)
	v_max_f32_e32 v6, v6, v6
	v_max_f32_e32 v4, v4, v6
	ds_bpermute_b32 v6, v190, v5
	v_mul_f32_e32 v4, 0x41000000, v4
	s_waitcnt lgkmcnt(0)
	v_max_f32_e32 v6, v6, v6
	v_max_f32_e32 v5, v5, v6
	v_mul_f32_e32 v4, v5, v4
	v_mul_f32_e32 v240, 0x3fb8aa3b, v4
	v_fmaak_f32 v5, 2.0, v4, 0x42000000
	global_load_dword v4, v131, s[14:15]
	s_mov_b64 s[14:15], -1
	s_and_saveexec_b64 s[22:23], vcc
	s_cbranch_execz .LBB0_929
	s_lshl_b32 s8, s4, 18
	v_lshl_or_b32 v130, v191, 11, s8
	v_lshl_add_u64 v[6:7], s[34:35], 0, v[130:131]
	v_lshl_add_u64 v[6:7], s[0:1], 2, v[6:7]
	global_load_dword v6, v[6:7], off offset:2016
	s_waitcnt vmcnt(0)
	v_sub_f32_e32 v6, v4, v6
	v_cmp_ge_f32_e64 s[18:19], v6, -v5
	s_orn2_b64 s[18:19], s[18:19], exec

; #define WAITV(n) do { switch (n) { WV_(0) WV_(1) WV_(2) WV_(3) WV_(4) WV_(5) default: asm volatile("s_waitcnt vmcnt(6)" ::: "memory"); break; } } while (0)
; #define LBAR() asm volatile("s_waitcnt lgkmcnt(0)\n\ts_barrier" ::: "memory")
; #define KREAD(rel) { const lds_cptr kp = kp0 + ((rel) % NS) * KSLOT; \
;         _Pragma("unroll") for (int d0 = 0; d0 < NQ; ++d0) { kf[2 * d0] = *(const LAS bf16x8*)(kp + d0 * 2048); kf[2 * d0 + 1] = *(const LAS bf16x8*)(kp + d0 * 2048 + 512); } }
; #define ROWMAX(dst) do { float ma = MX3(c0[0], c0[1], c1[0]), mb = MX3(c0[2], c0[3], c1[1]); ma = MX3(ma, c1[2], c1[3]); \
;         _Pragma("unroll") for (int r = 4; r < 16; r += 4) { ma = MX3(ma, c0[r], c0[r + 1]); mb = MX3(mb, c0[r + 2], c0[r + 3]); ma = MX3(ma, c1[r], c1[r + 1]); mb = MX3(mb, c1[r + 2], c1[r + 3]); } \
;         dst = swapmax(fmaxf(ma, mb)); } while (0)
; #define CIPART(rel, g) do { const float mneg = (t0 + (rel) > tw_last) ? -INFINITY : -mhat; const LAS float* Gt = Gl + (rel) * 64 + 4 * hi + ((g) >> 2) * 32 + 8 * ((g) & 3); const f32x4 gg = *(const LAS f32x4*)Gt; \
;         _Pragma("unroll") for (int i = 0; i < 4; ++i) { if ((g) < 4) c0[4 * ((g) & 3) + i] = gg[i] + mneg; else c1[4 * ((g) & 3) + i] = gg[i] + mneg; } } while (0)
; template <bool FOX>
; __device__ __forceinline__ void attn_unit(const Args& A, int b, int h, int qb, LAS char* shm, LAS float* dg) {
;     ...
;     { float rm; ROWMAX(rm); mhat = rm;
;       if constexpr (!FOX) {
; #pragma unroll
;           for (int r = 0; r < 16; ++r) negm[r] = -rm;
;           asm volatile("" : "+v"(negm)); }
; #pragma unroll
;         for (int r = 0; r < 16; ++r) { pp0[r] = __builtin_amdgcn_exp2f(c0[r] - rm); pp1[r] = __builtin_amdgcn_exp2f(c1[r] - rm); } }
;     KREAD(1);
;     if constexpr (FOX) {
; #pragma unroll
;         for (int g = 0; g < 8; ++g) CIPART(1, g); }
;     WAITV(nK + 2);
;     LBAR();
;     const int t_end = (tw_last - t0 + 2 < nti) ? tw_last - t0 + 2 : nti;
.LBB0_948:
	v_lshlrev_b32_e32 v30, 1, v128
	v_lshrrev_b32_e32 v32, 2, v128
	v_and_b32_e32 v30, 32, v30
	v_lshlrev_b32_e32 v31, 3, v128
	v_and_or_b32 v32, v32, 3, v197
	v_and_b32_e32 v31, 24, v31
	v_lshlrev_b32_e32 v32, 6, v32
	v_add_u32_e32 v30, s70, v30
	v_add3_u32 v198, v30, v31, v32
	v_max_f32_e32 v30, v21, v21
	v_max_f32_e32 v31, v20, v20
	v_max_f32_e32 v30, v31, v30
	v_max3_f32 v31, v38, v39, v37
	v_max3_f32 v30, v30, v36, v22
	v_max3_f32 v30, v30, v23, v4
	v_max3_f32 v31, v31, v8, v9
	v_max3_f32 v30, v30, v5, v6
	v_max3_f32 v31, v31, v10, v11
	v_max3_f32 v30, v30, v7, v28
	v_max3_f32 v31, v31, v26, v27
	v_max3_f32 v30, v30, v29, v44
	v_max3_f32 v31, v31, v24, v25
	v_max3_f32 v30, v30, v45, v12
	v_max3_f32 v31, v31, v14, v15
	v_max3_f32 v30, v30, v13, v16
	v_max3_f32 v31, v31, v18, v19
	v_max3_f32 v30, v30, v17, v31
	v_mov_b32_e32 v31, v30
	s_nop 1
	v_permlane32_swap_b32_e32 v30, v31
	v_max_f32_e32 v31, v31, v31
	v_max_f32_e32 v30, v30, v30
	v_max_f32_e32 v235, v30, v31
	v_add_u32_e32 v30, s8, v129
	v_subrev_u32_e32 v30, s26, v30
	v_lshl_add_u32 v30, v30, 2, s97
	ds_read_b32 v30, v30
	v_mov_b32_e32 v31, 0x42480000
	v_cmp_le_f32_e32 vcc, v240, v31
	s_waitcnt lgkmcnt(0)
	v_add_f32_e32 v30, v30, v240
	s_nop 0
	v_cndmask_b32_e32 v235, v235, v30, vcc
	s_cmp_lg_u64 vcc, 0
	s_cselect_b32 s99, 1, 0
	v_sub_f32_e32 v4, v4, v235
	v_exp_f32_e32 v56, v4
	v_sub_f32_e32 v4, v6, v235
	v_exp_f32_e32 v40, v4
	v_sub_f32_e32 v4, v5, v235
	v_exp_f32_e32 v57, v4
	v_sub_f32_e32 v4, v7, v235
	v_exp_f32_e32 v41, v4
	v_sub_f32_e32 v4, v8, v235
	v_exp_f32_e32 v58, v4
	v_sub_f32_e32 v4, v10, v235
	v_exp_f32_e32 v42, v4
	v_sub_f32_e32 v4, v9, v235
	v_exp_f32_e32 v59, v4
	v_sub_f32_e32 v4, v11, v235
	v_exp_f32_e32 v43, v4
	v_sub_f32_e32 v4, v28, v235
	v_exp_f32_e32 v60, v4
	v_sub_f32_e32 v4, v44, v235
	v_exp_f32_e32 v44, v4
	v_sub_f32_e32 v4, v29, v235
	v_exp_f32_e32 v61, v4
	v_sub_f32_e32 v4, v45, v235
	v_exp_f32_e32 v45, v4
	v_sub_f32_e32 v4, v26, v235
	v_exp_f32_e32 v62, v4
	v_sub_f32_e32 v4, v24, v235
	v_exp_f32_e32 v46, v4
	v_sub_f32_e32 v4, v27, v235
	v_exp_f32_e32 v63, v4
	v_sub_f32_e32 v4, v25, v235
	v_sub_f32_e32 v20, v20, v235
	v_exp_f32_e32 v47, v4
	v_sub_f32_e32 v4, v12, v235
	v_exp_f32_e32 v52, v20
	v_sub_f32_e32 v20, v36, v235
	v_exp_f32_e32 v64, v4
	v_sub_f32_e32 v4, v16, v235
	v_exp_f32_e32 v36, v20
	v_sub_f32_e32 v20, v21, v235
	v_exp_f32_e32 v48, v4
	v_sub_f32_e32 v4, v13, v235
	v_exp_f32_e32 v53, v20
	v_sub_f32_e32 v20, v37, v235
	v_exp_f32_e32 v65, v4
	v_sub_f32_e32 v4, v17, v235
	v_exp_f32_e32 v37, v20
	v_sub_f32_e32 v20, v38, v235
	v_exp_f32_e32 v49, v4
	v_sub_f32_e32 v4, v14, v235
	v_exp_f32_e32 v54, v20
	v_sub_f32_e32 v20, v22, v235
	v_exp_f32_e32 v66, v4
	v_sub_f32_e32 v4, v18, v235
	v_exp_f32_e32 v38, v20
	v_sub_f32_e32 v20, v39, v235
	v_exp_f32_e32 v50, v4
	v_sub_f32_e32 v4, v15, v235
	v_exp_f32_e32 v55, v20
	v_sub_f32_e32 v20, v23, v235
	v_exp_f32_e32 v67, v4
	v_sub_f32_e32 v4, v19, v235
	v_lshl_add_u32 v32, v197, 2, s92
	v_exp_f32_e32 v39, v20
	v_exp_f32_e32 v51, v4
	ds_read_b128 v[150:153], v196 offset:8192
	ds_read_b128 v[124:127], v196 offset:8704
	ds_read_b128 v[142:145], v196 offset:10240
	ds_read_b128 v[116:119], v196 offset:10752
	ds_read_b128 v[154:157], v196 offset:12288
	ds_read_b128 v[138:141], v196 offset:12800
	ds_read_b128 v[146:149], v196 offset:14336
	ds_read_b128 v[120:123], v196 offset:14848
	ds_read_b128 v[4:7], v32
	ds_read_b128 v[8:11], v32 offset:32
	ds_read_b128 v[12:15], v32 offset:64
	ds_read_b128 v[16:19], v32 offset:96
	ds_read_b128 v[20:23], v32 offset:128
	ds_read_b128 v[24:27], v32 offset:160
	ds_read_b128 v[28:31], v32 offset:192
	ds_read_b128 v[68:71], v32 offset:224
	s_lshr_b32 s6, s27, 6
	s_and_b32 s7, s7, 0x3fffffc0
	s_waitcnt vmcnt(3)
	s_sub_i32 s15, s33, s14
	s_sub_i32 s6, s6, s14
	s_lshl_b32 s7, s7, 2
	s_waitcnt lgkmcnt(0)
	s_barrier
	s_add_i32 s15, s15, 2
	s_add_i32 s19, s96, s7
	s_min_i32 s7, s15, s6
	v_mov_b32_e32 v35, 0
	s_cmp_lt_i32 s7, 2
	v_cmp_gt_u32_e64 s[22:23], 32, v191
	v_lshl_add_u32 v194, v129, 2, s19
	v_lshl_add_u32 v193, v197, 2, s19
	s_cbranch_scc1 .LBB0_982
	s_cmp_gt_i32 s33, s14
	s_cselect_b64 s[24:25], -1, 0
	s_cmp_gt_i32 s6, 4
	v_cndmask_b32_e64 v32, v2, -v235, s[24:25]
	s_cselect_b64 s[24:25], -1, 0
	s_add_i32 s40, s14, 4
	v_readlane_b32 s19, v254, 48
	s_ashr_i32 s41, s40, 31
	s_waitcnt lgkmcnt(7)
	v_pk_add_f32 v[84:85], v[32:33], v[4:5] op_sel_hi:[0,1]
	v_lshl_add_u32 v242, v192, 4, s19
	s_sub_i32 s19, s8, 64
	s_lshl_b64 s[40:41], s[40:41], 13
	v_add_u32_e32 v4, s19, v129
	v_mov_b32_e32 v195, 0
	s_waitcnt lgkmcnt(0)
	v_pk_add_f32 v[82:83], v[32:33], v[70:71] op_sel_hi:[0,1]
	v_pk_add_f32 v[78:79], v[32:33], v[30:31] op_sel_hi:[0,1]
	v_pk_add_f32 v[74:75], v[32:33], v[26:27] op_sel_hi:[0,1]
	v_pk_add_f32 v[70:71], v[32:33], v[22:23] op_sel_hi:[0,1]
	v_pk_add_f32 v[80:81], v[32:33], v[68:69] op_sel_hi:[0,1]
	v_pk_add_f32 v[76:77], v[32:33], v[28:29] op_sel_hi:[0,1]
	v_pk_add_f32 v[72:73], v[32:33], v[24:25] op_sel_hi:[0,1]
	v_pk_add_f32 v[68:69], v[32:33], v[20:21] op_sel_hi:[0,1]
	v_pk_add_f32 v[98:99], v[32:33], v[18:19] op_sel_hi:[0,1]
	v_pk_add_f32 v[94:95], v[32:33], v[14:15] op_sel_hi:[0,1]
	v_pk_add_f32 v[90:91], v[32:33], v[10:11] op_sel_hi:[0,1]
	v_pk_add_f32 v[86:87], v[32:33], v[6:7] op_sel_hi:[0,1]
	v_pk_add_f32 v[96:97], v[32:33], v[16:17] op_sel_hi:[0,1]
	v_pk_add_f32 v[92:93], v[32:33], v[12:13] op_sel_hi:[0,1]
	v_pk_add_f32 v[88:89], v[32:33], v[8:9] op_sel_hi:[0,1]
	v_lshl_add_u64 v[188:189], v[132:133], 0, s[40:41]
	v_subrev_u32_e32 v243, s26, v4
	s_add_i32 s19, s26, 0x7f
	s_mov_b32 s53, 1
	s_mov_b32 s38, 0x8000
	s_mov_b32 s52, 0
	v_mov_b32_e32 v4, 0
	v_mov_b32_e32 v5, v195
	v_mov_b32_e32 v6, v195
	v_mov_b32_e32 v7, v195
	v_mov_b32_e32 v8, v195
	v_mov_b32_e32 v9, v195
	v_mov_b32_e32 v10, v195
	v_mov_b32_e32 v11, v195
	v_mov_b32_e32 v12, v195
	v_mov_b32_e32 v13, v195
	v_mov_b32_e32 v14, v195
	v_mov_b32_e32 v15, v195
	v_mov_b32_e32 v16, v195
	v_mov_b32_e32 v17, v195
	v_mov_b32_e32 v18, v195
	v_mov_b32_e32 v19, v195
	v_mov_b32_e32 v20, 0
	v_mov_b32_e32 v21, v195
	v_mov_b32_e32 v22, v195
	v_mov_b32_e32 v23, v195
	v_mov_b32_e32 v24, v195
	v_mov_b32_e32 v25, v195
	v_mov_b32_e32 v26, v195
	v_mov_b32_e32 v27, v195
	v_mov_b32_e32 v28, v195
	v_mov_b32_e32 v29, v195
	v_mov_b32_e32 v30, v195
	v_mov_b32_e32 v31, v195
	v_mov_b32_e32 v32, v195
	v_mov_b32_e32 v33, v195
	v_mov_b32_e32 v34, v195
	v_mov_b32_e32 v35, v195

; #define ROWMAX(dst) do { float ma = MX3(c0[0], c0[1], c1[0]), mb = MX3(c0[2], c0[3], c1[1]); ma = MX3(ma, c1[2], c1[3]); \
;         _Pragma("unroll") for (int r = 4; r < 16; r += 4) { ma = MX3(ma, c0[r], c0[r + 1]); mb = MX3(mb, c0[r + 2], c0[r + 3]); ma = MX3(ma, c1[r], c1[r + 1]); mb = MX3(mb, c1[r + 2], c1[r + 3]); } \
;         dst = swapmax(fmaxf(ma, mb)); } while (0)
; #define MASKONLY(rel) do { if constexpr (FOX) { const int tt_ = t0 + (rel); if (64 * tt_ + 63 > qw) { const int qrel = qw + r32 - 64 * tt_; \
;             _Pragma("unroll") for (int r = 0; r < 16; ++r) { const int kv = crow(r, hi); c0[r] = kv > qrel ? -INFINITY : c0[r]; c1[r] = kv + 32 > qrel ? -INFINITY : c1[r]; } } } } while (0)
; template <bool FOX>
; __device__ __forceinline__ void attn_unit(const Args& A, int b, int h, int qb, LAS char* shm, LAS float* dg) {
;     ...
;         MASKONLY(t);
;         float rm; ROWMAX(rm);
;         bool resc = false;
;         if (__any(rm > THR)) { const float dl = fmaxf(rm, 0.f); mhat += dl;
; #pragma unroll
;             for (int r = 0; r < 16; ++r) { c0[r] -= dl; c1[r] -= dl; }
;             if constexpr (!FOX) {
; #pragma unroll
;                 for (int r = 0; r < 16; ++r) negm[r] = -mhat;
;                 asm volatile("" : "+v"(negm)); }
;             const float f = __builtin_amdgcn_exp2f(-dl); lrun *= f; if (hi == 0) wsf[r32] = f; resc = true; }
.LBB0_958:
	v_add_f32_e32 v36, v36, v37
	v_add_f32_e32 v195, v195, v36
	s_cmp_lg_u32 s99, 0
	s_cbranch_scc1 .Lfox_fixed_ref
	v_max_f32_e32 v36, v85, v85
	v_max_f32_e32 v37, v84, v84
	v_max_f32_e32 v36, v37, v36
	v_max3_f32 v37, v86, v87, v69
	v_max3_f32 v36, v36, v68, v70
	v_max3_f32 v36, v36, v71, v88
	v_max3_f32 v37, v37, v90, v91
	v_max3_f32 v36, v36, v89, v72
	v_max3_f32 v37, v37, v74, v75
	v_max3_f32 v36, v36, v73, v92
	v_max3_f32 v37, v37, v94, v95
	v_max3_f32 v36, v36, v93, v76
	v_max3_f32 v37, v37, v78, v79
	v_max3_f32 v36, v36, v77, v96
	v_max3_f32 v37, v37, v98, v99
	v_max3_f32 v36, v36, v97, v80
	v_max3_f32 v37, v37, v82, v83
	v_max3_f32 v36, v36, v81, v37
	v_mov_b32_e32 v37, v36
	s_nop 1
	v_permlane32_swap_b32_e32 v36, v37
	v_max_f32_e32 v37, v37, v37
	v_max_f32_e32 v36, v36, v36
	v_max_f32_e32 v36, v36, v37
	v_cmp_lt_f32_e32 vcc, s95, v36
	s_cmp_lg_u64 vcc, 0
	s_cselect_b64 s[44:45], -1, 0
	s_cbranch_vccz .LBB0_962
	v_max_f32_e32 v36, v36, v36
	v_max_f32_e32 v37, 0, v36
	v_exp_f32_e64 v36, -v37
	s_and_saveexec_b64 s[46:47], s[22:23]
	ds_write_b32 v194, v36
	s_or_b64 exec, exec, s[46:47]
	v_sub_f32_e32 v99, v99, v37
	v_sub_f32_e32 v98, v98, v37
	v_sub_f32_e32 v97, v97, v37
	v_sub_f32_e32 v96, v96, v37
	v_sub_f32_e32 v95, v95, v37
	v_sub_f32_e32 v94, v94, v37
	v_sub_f32_e32 v93, v93, v37
	v_sub_f32_e32 v92, v92, v37
	v_sub_f32_e32 v91, v91, v37
	v_sub_f32_e32 v90, v90, v37
	v_sub_f32_e32 v89, v89, v37
	v_sub_f32_e32 v88, v88, v37
	v_sub_f32_e32 v87, v87, v37
	v_sub_f32_e32 v86, v86, v37
	v_sub_f32_e32 v85, v85, v37
	v_sub_f32_e32 v84, v84, v37
	v_sub_f32_e32 v83, v83, v37
	v_sub_f32_e32 v82, v82, v37
	v_sub_f32_e32 v81, v81, v37
	v_sub_f32_e32 v80, v80, v37
	v_sub_f32_e32 v79, v79, v37
	v_sub_f32_e32 v78, v78, v37
	v_sub_f32_e32 v77, v77, v37
	v_sub_f32_e32 v76, v76, v37
	v_sub_f32_e32 v75, v75, v37
	v_sub_f32_e32 v74, v74, v37
	v_sub_f32_e32 v73, v73, v37
	v_sub_f32_e32 v72, v72, v37
	v_sub_f32_e32 v71, v71, v37
	v_sub_f32_e32 v70, v70, v37
	v_sub_f32_e32 v69, v69, v37
	v_sub_f32_e32 v68, v68, v37
	v_add_f32_e32 v235, v235, v37
	v_mul_f32_e32 v195, v195, v36
	s_branch .LBB0_962
.Lfox_fixed_ref:
	s_mov_b64 s[44:45], 0
